# v43 with K-loop heads pinned at byte offsets mod 64: in-proj 4, proj 48, out 60, gate_up 52, down 60 (padding in never-executed gaps)
# speedup vs baseline: 1.0280x; 1.0280x over previous
; #define PG8_STAGE(bufoff, gbase, voff) do { _Pragma("unroll") for (int _i = 0; _i < 2; ++_i) \
;         __builtin_amdgcn_global_load_lds((const unsigned*)((const char*)(gbase) + (voff)[_i]), (PG8_LAS unsigned*)(lds + (bufoff) + ldsw + _i * 8192), 16, 0, 0); } while (0)
; #define PG8_LDA(dst, b, h) do { _Pragma("unroll") for (int m = 0; m < 4; ++m) _Pragma("unroll") for (int k = 0; k < 2; ++k) dst[m][k] = *(const PG8_LAS bf16x8*)(lds + PG8_SA(b, h) + aoff + m * 2048 + k * 1024); } while (0)
; #define PG8_LDB(dst, b, h) do { _Pragma("unroll") for (int n = 0; n < 2; ++n) _Pragma("unroll") for (int k = 0; k < 2; ++k) dst[n][k] = *(const PG8_LAS bf16x8*)(lds + PG8_SB(b, h) + boff + n * 2048 + k * 1024); } while (0)
; #define PG8_MMA(ai, bj, At, Bt) do { __builtin_amdgcn_s_setprio(1); _Pragma("unroll") for (int m = 0; m < 4; ++m) _Pragma("unroll") for (int n = 0; n < 2; ++n) _Pragma("unroll") for (int k = 0; k < 2; ++k) \
;         acc[ai][bj][m][n] = __builtin_amdgcn_mfma_f32_16x16x32_bf16(Bt[n][k], At[m][k], acc[ai][bj][m][n], 0, 0, 0); __builtin_amdgcn_s_setprio(0); } while (0)
; #define PG8_WAIT_V(n) asm volatile("s_waitcnt vmcnt(" #n ")" ::: "memory")
; #define PG8_WAIT_L(n) asm volatile("s_waitcnt lgkmcnt(" #n ")" ::: "memory")
; #define PG8_BAR __builtin_amdgcn_s_barrier()
; #define PG8_SCHED __builtin_amdgcn_sched_barrier(0)
; template <class Epi, class Sched, bool ALIGN_EPI = false, bool SP2 = false>
; __device__ __forceinline__ void gemm_phase(PG8_LAS unsigned char* lds, const Gemm g, const Sched& S, const Epi& E) {
;     ...
;             PG8_LDB(B0, 0, 0); PG8_LDB(B1, 0, 1); PG8_SCHED; PG8_LDA(At, 0, 0); PG8_STAGE(PG8_SA(1, 1), a1 + hstep, voffA);
;     ...
;             if (PROBE_KIND == 18 && t == 0 && ui > 0 && g.probe) { const unsigned long long tq_ = __builtin_amdgcn_s_memrealtime(); PG8_WAIT_V(8); pg8_probe_acc += (unsigned)(__builtin_amdgcn_s_memrealtime() - tq_); }
;     ...
;             PG8_WAIT_V(8); PG8_WAIT_L(0); PG8_BAR; PG8_MMA(0, 0, At, B0); PG8_MMA(0, 1, At, B1); PG8_BAR; PG8_SCHED;
;             PG8_LDA(At, 0, 1); PG8_STAGE(PG8_SB(0, 0), b2, voffB); PG8_STAGE(PG8_SB(0, 1), b2 + hstep, voffB); PG8_STAGE(PG8_SA(0, 0), a2, voffA);
;             PG8_WAIT_V(8); PG8_WAIT_L(0); PG8_BAR; if (cur.half == 0) { PG8_MMA(1, 0, At, B0); PG8_MMA(1, 1, At, B1); } PG8_BAR; PG8_SCHED;
.Lpj_ip_1:
	s_waitcnt lgkmcnt(0)
	s_barrier
	s_setprio 1
	s_waitcnt lgkmcnt(0)
	v_mfma_f32_16x16x32_bf16 v[128:131], v[132:135], v[182:185], 0
	v_mfma_f32_16x16x32_bf16 v[124:127], v[140:143], v[182:185], 0
	v_mfma_f32_16x16x32_bf16 v[112:115], v[132:135], v[190:193], 0
	v_mfma_f32_16x16x32_bf16 v[108:111], v[140:143], v[190:193], 0
	v_mfma_f32_16x16x32_bf16 v[96:99], v[132:135], v[198:201], 0
	v_mfma_f32_16x16x32_bf16 v[92:95], v[140:143], v[198:201], 0
	v_mfma_f32_16x16x32_bf16 v[80:83], v[132:135], v[212:215], 0
	v_mfma_f32_16x16x32_bf16 v[76:79], v[140:143], v[212:215], 0
	v_mfma_f32_16x16x32_bf16 v[128:131], v[136:139], v[186:189], v[128:131]
	v_mfma_f32_16x16x32_bf16 v[124:127], v[144:147], v[186:189], v[124:127]
	v_mfma_f32_16x16x32_bf16 v[112:115], v[136:139], v[194:197], v[112:115]
	v_mfma_f32_16x16x32_bf16 v[108:111], v[144:147], v[194:197], v[108:111]
	v_mfma_f32_16x16x32_bf16 v[96:99], v[136:139], v[208:211], v[96:99]
	v_mfma_f32_16x16x32_bf16 v[92:95], v[144:147], v[208:211], v[92:95]
	v_mfma_f32_16x16x32_bf16 v[80:83], v[136:139], v[216:219], v[80:83]
	v_mfma_f32_16x16x32_bf16 v[76:79], v[144:147], v[216:219], v[76:79]
	s_setprio 0
	s_setprio 1
	v_mfma_f32_16x16x32_bf16 v[120:123], v[148:151], v[182:185], 0
	v_mfma_f32_16x16x32_bf16 v[116:119], v[156:159], v[182:185], 0
	v_mfma_f32_16x16x32_bf16 v[104:107], v[148:151], v[190:193], 0
	v_mfma_f32_16x16x32_bf16 v[100:103], v[156:159], v[190:193], 0
	v_mfma_f32_16x16x32_bf16 v[88:91], v[148:151], v[198:201], 0
	v_mfma_f32_16x16x32_bf16 v[84:87], v[156:159], v[198:201], 0
	v_mfma_f32_16x16x32_bf16 v[72:75], v[148:151], v[212:215], 0
	v_mfma_f32_16x16x32_bf16 v[68:71], v[156:159], v[212:215], 0
	v_mfma_f32_16x16x32_bf16 v[120:123], v[152:155], v[186:189], v[120:123]
	v_mfma_f32_16x16x32_bf16 v[116:119], v[160:163], v[186:189], v[116:119]
	v_mfma_f32_16x16x32_bf16 v[104:107], v[152:155], v[194:197], v[104:107]
	v_mfma_f32_16x16x32_bf16 v[100:103], v[160:163], v[194:197], v[100:103]
	v_mfma_f32_16x16x32_bf16 v[88:91], v[152:155], v[208:211], v[88:91]
	v_mfma_f32_16x16x32_bf16 v[84:87], v[160:163], v[208:211], v[84:87]
	v_mfma_f32_16x16x32_bf16 v[72:75], v[152:155], v[216:219], v[72:75]
	v_mfma_f32_16x16x32_bf16 v[68:71], v[160:163], v[216:219], v[68:71]
	s_setprio 0
	s_barrier
	s_add_i32 s61, s61, s27
	v_lshl_add_u64 v[228:229], s[0:1], 0, v[166:167]
	s_mov_b32 m0, s61
	ds_read_b128 v[182:185], v206 offset:16384
	ds_read_b128 v[186:189], v206 offset:17408
	ds_read_b128 v[190:193], v206 offset:18432
	ds_read_b128 v[194:197], v206 offset:19456
	ds_read_b128 v[198:201], v206 offset:20480
	ds_read_b128 v[208:211], v206 offset:21504
	ds_read_b128 v[212:215], v206 offset:22528
	ds_read_b128 v[216:219], v206 offset:23552
	global_load_lds_dwordx4 v[228:229], off
	s_add_i32 m0, s61, 0x2000
	s_add_u32 s78, s0, 0x40000
	v_lshl_add_u64 v[230:231], s[0:1], 0, v[170:171]
	s_addc_u32 s79, s1, 0
	s_add_i32 s61, s63, s27
	global_load_lds_dwordx4 v[230:231], off
	v_lshl_add_u64 v[232:233], s[78:79], 0, v[166:167]
	s_mov_b32 m0, s61
	v_lshl_add_u64 v[234:235], s[10:11], 0, v[168:169]
	global_load_lds_dwordx4 v[232:233], off
	v_lshl_add_u64 v[232:233], s[78:79], 0, v[170:171]
	s_add_i32 m0, s61, 0x2000
	s_nop 0
	global_load_lds_dwordx4 v[232:233], off
	v_lshl_add_u64 v[232:233], s[10:11], 0, v[164:165]
	s_mov_b32 m0, s19
	s_nop 0
	global_load_lds_dwordx4 v[232:233], off
	s_mov_b32 m0, s30
	s_nop 0
	global_load_lds_dwordx4 v[234:235], off
	s_cmp_eq_u32 s32, 0
	s_cbranch_scc1 .Lpw_ip_2
	s_waitcnt vmcnt(24)
	s_branch .Lpj_ip_2
	.p2align 6
	s_nop 0

; #define PG8_LAS __attribute__((address_space(3)))
;     __device__ __forceinline__ void a_ready(const Unit&) const { if (++ncall == 3 && sig != nullptr && threadIdx.x == 0) __hip_atomic_fetch_add(sig, 1u, __ATOMIC_RELAXED, __HIP_MEMORY_SCOPE_AGENT); }
; __device__ __forceinline__ f32x4 load_row_partials(const float* rsp, int pm, int tid) { f32x4 p = {0.f, 0.f, 0.f, 0.f}; if (tid < BM) p = *(const f32x4*)(rsp + (size_t)(pm * BM + tid) * 4); return p; }
; #define PG8_STAGE(bufoff, gbase, voff) do { _Pragma("unroll") for (int _i = 0; _i < 2; ++_i) \
;         __builtin_amdgcn_global_load_lds((const unsigned*)((const char*)(gbase) + (voff)[_i]), (PG8_LAS unsigned*)(lds + (bufoff) + ldsw + _i * 8192), 16, 0, 0); } while (0)
; #define PG8_WAIT_V(n) asm volatile("s_waitcnt vmcnt(" #n ")" ::: "memory")
; #define PG8_BAR __builtin_amdgcn_s_barrier()
; template <class Epi, class Sched, bool ALIGN_EPI = false, bool SP2 = false>
; __device__ __forceinline__ void gemm_phase(PG8_LAS unsigned char* lds, const Gemm g, const Sched& S, const Epi& E) {
;     ...
;     f32x4 rowp_ = {0.f, 0.f, 0.f, 0.f}; if constexpr (Epi::ROWSCALE) rowp_ = load_row_partials(E.rsp, cur.pm, tid);
;     f32x4 acc[2][2][4][2];
; #pragma unroll
;     for (int a = 0; a < 2; ++a)
; #pragma unroll
;         for (int b = 0; b < 2; ++b)
; #pragma unroll
;             for (int m = 0; m < 4; ++m)
; #pragma unroll
;                 for (int n = 0; n < 2; ++n) acc[a][b][m][n] = (f32x4){0.f, 0.f, 0.f, 0.f};
;     bf16x8 At[4][2], B0[2][2], B1[2][2];
;     const char* cA = (const char*)g.A + (size_t)cur.pm * tstep + (cur.half == 2 ? hstep : (size_t)0); const char* cB = (const char*)g.Bt + (size_t)cur.pn * tstep;
;     S.a_ready(cur);
;     if constexpr (SP2) {
;         PG8_STAGE(PG8_SB(0, 0), cB, voffB); PG8_STAGE(PG8_SB(0, 1), cB + hstep, voffB); PG8_STAGE(PG8_SA(0, 0), cA, voffA); PG8_STAGE(PG8_SA(0, 1), cA + hstep, voffA);
;         if (wr == 1) PG8_BAR;
;         PG8_WAIT_V(2); PG8_BAR;
;         if constexpr (Epi::ROWSCALE) stage_row_factors(rowp_, (PG8_LAS float*)E.rsl, tid);
;         PG8_STAGE(PG8_SB(1, 0), cB + kstep, voffB); PG8_STAGE(PG8_SA(1, 0), cA + kstep, voffA); PG8_STAGE(PG8_SB(1, 1), cB + hstep + kstep, voffB);
;         PG8_WAIT_V(6); PG8_BAR;
.LBB0_1125:
	s_add_u32 s34, s12, 0x10000000
	s_addc_u32 s35, s13, 0
	s_add_u32 s10, s12, 0x11000000
	s_addc_u32 s11, s13, 0
	s_add_u32 s12, s12, 0x12000000
	s_addc_u32 s13, s13, 0
	s_lshl_b32 s5, s18, 5
	s_and_b32 s5, s5, 0x60
	s_add_i32 m0, s28, 0x18000
	v_lshl_add_u64 v[10:11], v[10:11], 0, s[42:43]
	s_lshl_b32 s1, s17, 13
	s_waitcnt lgkmcnt(0)
	s_lshl_b32 s20, s5, 7
	s_waitcnt vmcnt(2)
	s_barrier
	global_load_lds_dwordx4 v[10:11], off
	v_lshl_add_u64 v[8:9], v[8:9], 0, s[42:43]
	s_add_i32 m0, s28, 0x1a000
	s_add_i32 s36, s28, 0x8000
	s_add_i32 s40, s28, 0xa000
	global_load_lds_dwordx4 v[8:9], off
	v_lshl_add_u64 v[4:5], v[4:5], 0, s[42:43]
	s_mov_b32 m0, s36
	s_add_u32 s18, s14, 0x20080
	global_load_lds_dwordx4 v[4:5], off
	v_lshl_add_u64 v[4:5], v[6:7], 0, s[42:43]
	s_mov_b32 m0, s40
	s_addc_u32 s19, s15, 0
	global_load_lds_dwordx4 v[4:5], off
	s_add_i32 m0, s28, 0x1c000
	v_lshl_add_u64 v[4:5], s[18:19], 0, v[2:3]
	global_load_lds_dwordx4 v[4:5], off
	v_lshl_add_u64 v[4:5], s[18:19], 0, v[168:169]
	s_add_i32 m0, s28, 0x1e000
	v_mov_b32_e32 v7, v3
	global_load_lds_dwordx4 v[4:5], off
	v_lshrrev_b32_e32 v5, 1, v12
	v_and_b32_e32 v5, 24, v5
	v_and_b32_e32 v4, 15, v12
	v_lshlrev_b32_e32 v6, 1, v5
	v_lshl_or_b32 v200, s17, 6, v4
	v_lshl_or_b32 v4, v4, 6, v6
	v_lshlrev_b32_e32 v6, 2, v12
	v_and_b32_e32 v6, 32, v6
	v_bitop3_b32 v8, v4, s1, v6 bitop3:0xde
	v_bitop3_b32 v201, v4, s20, v6 bitop3:0xde
	v_lshlrev_b32_e32 v4, 13, v13
	v_and_b32_e32 v4, 0xffffc000, v4
	v_or_b32_e32 v202, s5, v5
	v_lshl_add_u32 v4, v14, 10, v4
	v_and_b32_e32 v5, 1, v13
	v_lshl_or_b32 v4, v5, 6, v4
	v_lshl_add_u32 v170, v15, 1, v4
	v_lshlrev_b32_e32 v4, 13, v16
	v_and_b32_e32 v4, 0xffffc000, v4
	v_lshl_add_u32 v4, v17, 10, v4
	v_and_b32_e32 v5, 1, v16
	s_waitcnt vmcnt(6)
	v_lshl_or_b32 v4, v5, 6, v4
	v_mov_b32_e32 v6, v3
	s_cmpk_lt_u32 s16, 0x100
	v_lshl_add_u32 v172, v18, 1, v4
	v_mov_b32_e32 v4, v3
	v_mov_b32_e32 v5, v3
	v_add_u32_e32 v203, 0, v8
	v_mov_b64_e32 v[10:11], v[6:7]
	v_mov_b64_e32 v[22:23], v[6:7]
	v_mov_b64_e32 v[26:27], v[6:7]
	v_mov_b64_e32 v[46:47], v[6:7]
	v_mov_b64_e32 v[50:51], v[6:7]
	v_mov_b64_e32 v[78:79], v[6:7]
	v_mov_b64_e32 v[82:83], v[6:7]
	v_mov_b64_e32 v[14:15], v[6:7]
	v_mov_b64_e32 v[18:19], v[6:7]
	v_mov_b64_e32 v[30:31], v[6:7]
	v_mov_b64_e32 v[34:35], v[6:7]
	v_mov_b64_e32 v[62:63], v[6:7]
	v_mov_b64_e32 v[66:67], v[6:7]
	v_mov_b64_e32 v[94:95], v[6:7]
	v_mov_b64_e32 v[98:99], v[6:7]
	v_mov_b64_e32 v[110:111], v[6:7]
	v_mov_b64_e32 v[114:115], v[6:7]
	v_mov_b64_e32 v[142:143], v[6:7]
	v_mov_b64_e32 v[146:147], v[6:7]
	v_mov_b64_e32 v[150:151], v[6:7]
	v_mov_b64_e32 v[154:155], v[6:7]
	v_mov_b64_e32 v[158:159], v[6:7]
	v_mov_b64_e32 v[162:163], v[6:7]
	v_mov_b64_e32 v[126:127], v[6:7]
	v_mov_b64_e32 v[130:131], v[6:7]
	v_mov_b64_e32 v[118:119], v[6:7]
	v_mov_b64_e32 v[122:123], v[6:7]
	v_mov_b64_e32 v[86:87], v[6:7]
	v_mov_b64_e32 v[90:91], v[6:7]
	v_mov_b64_e32 v[54:55], v[6:7]
	v_mov_b64_e32 v[58:59], v[6:7]
	s_cselect_b64 s[16:17], -1, 0
	v_mov_b32_e32 v171, v3
	v_mov_b32_e32 v173, v3
	s_mov_b32 s1, 0
	v_mov_b64_e32 v[8:9], v[4:5]
	v_mov_b64_e32 v[20:21], v[4:5]
	v_mov_b64_e32 v[24:25], v[4:5]
	v_mov_b64_e32 v[44:45], v[4:5]
	v_mov_b64_e32 v[48:49], v[4:5]
	v_mov_b64_e32 v[76:77], v[4:5]
	v_mov_b64_e32 v[80:81], v[4:5]
	v_mov_b64_e32 v[12:13], v[4:5]
	v_mov_b64_e32 v[16:17], v[4:5]
	v_mov_b64_e32 v[28:29], v[4:5]
	v_mov_b64_e32 v[32:33], v[4:5]
	v_mov_b64_e32 v[60:61], v[4:5]
	v_mov_b64_e32 v[64:65], v[4:5]
	v_mov_b64_e32 v[92:93], v[4:5]
	v_mov_b64_e32 v[96:97], v[4:5]
	v_mov_b64_e32 v[108:109], v[4:5]
	v_mov_b64_e32 v[112:113], v[4:5]
	v_mov_b64_e32 v[140:141], v[4:5]
	v_mov_b64_e32 v[144:145], v[4:5]
	v_mov_b64_e32 v[148:149], v[4:5]
	v_mov_b64_e32 v[152:153], v[4:5]
	v_mov_b64_e32 v[156:157], v[4:5]
	v_mov_b64_e32 v[160:161], v[4:5]
	v_mov_b64_e32 v[124:125], v[4:5]
	v_mov_b64_e32 v[128:129], v[4:5]
	v_mov_b64_e32 v[116:117], v[4:5]
	v_mov_b64_e32 v[120:121], v[4:5]
	v_mov_b64_e32 v[84:85], v[4:5]
	v_mov_b64_e32 v[88:89], v[4:5]
	v_mov_b64_e32 v[52:53], v[4:5]
	v_mov_b64_e32 v[56:57], v[4:5]
	s_barrier
	s_branch .LBB0_1128
	.p2align 6
	s_nop 0
	s_nop 0
	s_nop 0
	s_nop 0
	s_nop 0
	s_nop 0
	s_nop 0
	s_nop 0
	s_nop 0
	s_nop 0

; __device__ __forceinline__ unsigned xb_ld(unsigned* p)              { return __hip_atomic_load(p, __ATOMIC_RELAXED, __HIP_MEMORY_SCOPE_AGENT); }
; __device__ __forceinline__ unsigned xb_add(unsigned* p, unsigned v) { return __hip_atomic_fetch_add(p, v, __ATOMIC_RELAXED, __HIP_MEMORY_SCOPE_AGENT); }
; #define XB_SPIN(cond, bar) do { unsigned _sp = 0; while (cond) { __builtin_amdgcn_s_sleep(1); \
;     if ((++_sp & 255u) == 0u) { if (xb_ld(&(bar)[XB_TMO])) break; if (_sp > XB_SPIN_CAP) { atomicAdd(&(bar)[XB_TMO], 1u); break; } } } } while (0)
; __device__ __forceinline__ void xcd_barrier(const XcdBarrier& b, const bool group_local = false, const bool xcc_only = false) {
;     ...
;         if (xcc_only && b.st[2] == 2u) {
;             if (old + 1u == (gen + 1u) * nloc) xb_add(&bar[XB_XGEN(b.x)], 1u);
;             else
;             XB_SPIN(xb_ld(&bar[XB_XSUB(b.x)]) < (gen + 1u) * nloc, bar);
;     ...
;             asm volatile("s_waitcnt vmcnt(0)" ::: "memory");
;     ...
;             __builtin_amdgcn_fence(__ATOMIC_ACQUIRE, "agent");
;             asm volatile("s_waitcnt vmcnt(0)" ::: "memory");
.LBB0_1263:
	s_add_u32 s4, s6, 0x2400
	s_addc_u32 s5, s7, 0
	v_mov_b64_e32 v[4:5], s[4:5]
	s_or_b64 s[12:13], s[12:13], exec
	s_or_b64 exec, exec, s[0:1]
	s_and_saveexec_b64 s[0:1], s[12:13]
	s_cbranch_execnz .LBB0_1106
	s_branch .LBB0_1107
	.p2align 6
	s_nop 0
	s_nop 0
	s_nop 0
	s_nop 0
	s_nop 0
	s_nop 0
	s_nop 0
	s_nop 0
	s_nop 0
	s_nop 0

; #define PG8_STAGE(bufoff, gbase, voff) do { _Pragma("unroll") for (int _i = 0; _i < 2; ++_i) \
;         __builtin_amdgcn_global_load_lds((const unsigned*)((const char*)(gbase) + (voff)[_i]), (PG8_LAS unsigned*)(lds + (bufoff) + ldsw + _i * 8192), 16, 0, 0); } while (0)
; #define PG8_LDA(dst, b, h) do { _Pragma("unroll") for (int m = 0; m < 4; ++m) _Pragma("unroll") for (int k = 0; k < 2; ++k) dst[m][k] = *(const PG8_LAS bf16x8*)(lds + PG8_SA(b, h) + aoff + m * 2048 + k * 1024); } while (0)
; #define PG8_LDB(dst, b, h) do { _Pragma("unroll") for (int n = 0; n < 2; ++n) _Pragma("unroll") for (int k = 0; k < 2; ++k) dst[n][k] = *(const PG8_LAS bf16x8*)(lds + PG8_SB(b, h) + boff + n * 2048 + k * 1024); } while (0)
; #define PG8_MMA(ai, bj, At, Bt) do { __builtin_amdgcn_s_setprio(1); _Pragma("unroll") for (int m = 0; m < 4; ++m) _Pragma("unroll") for (int n = 0; n < 2; ++n) _Pragma("unroll") for (int k = 0; k < 2; ++k) \
;         acc[ai][bj][m][n] = __builtin_amdgcn_mfma_f32_16x16x32_bf16(Bt[n][k], At[m][k], acc[ai][bj][m][n], 0, 0, 0); __builtin_amdgcn_s_setprio(0); } while (0)
; #define PG8_WAIT_V(n) asm volatile("s_waitcnt vmcnt(" #n ")" ::: "memory")
; #define PG8_WAIT_L(n) asm volatile("s_waitcnt lgkmcnt(" #n ")" ::: "memory")
; #define PG8_BAR __builtin_amdgcn_s_barrier()
; #define PG8_SCHED __builtin_amdgcn_sched_barrier(0)
; template <class Epi, class Sched, bool ALIGN_EPI = false, bool SP2 = false>
; __device__ __forceinline__ void gemm_phase(PG8_LAS unsigned char* lds, const Gemm g, const Sched& S, const Epi& E) {
;     ...
;             PG8_LDB(B0, 0, 0); PG8_LDB(B1, 0, 1); PG8_SCHED; PG8_LDA(At, 0, 0); PG8_STAGE(PG8_SA(1, 1), a1 + hstep, voffA);
;     ...
;             if (PROBE_KIND == 18 && t == 0 && ui > 0 && g.probe) { const unsigned long long tq_ = __builtin_amdgcn_s_memrealtime(); PG8_WAIT_V(8); pg8_probe_acc += (unsigned)(__builtin_amdgcn_s_memrealtime() - tq_); }
;     ...
;             PG8_WAIT_V(8); PG8_WAIT_L(0); PG8_BAR; PG8_MMA(0, 0, At, B0); PG8_MMA(0, 1, At, B1); PG8_BAR; PG8_SCHED;
;             PG8_LDA(At, 0, 1); PG8_STAGE(PG8_SB(0, 0), b2, voffB); PG8_STAGE(PG8_SB(0, 1), b2 + hstep, voffB); PG8_STAGE(PG8_SA(0, 0), a2, voffA);
;             PG8_WAIT_V(8); PG8_WAIT_L(0); PG8_BAR; if (cur.half == 0) { PG8_MMA(1, 0, At, B0); PG8_MMA(1, 1, At, B1); } PG8_BAR; PG8_SCHED;
.Lpj_gu_1:
	s_waitcnt lgkmcnt(0)
	s_barrier
	s_setprio 1
	s_waitcnt lgkmcnt(0)
	v_mfma_f32_16x16x32_bf16 v[128:131], v[142:145], v[180:183], 0
	v_mfma_f32_16x16x32_bf16 v[124:127], v[156:159], v[180:183], 0
	v_mfma_f32_16x16x32_bf16 v[112:115], v[142:145], v[188:191], 0
	v_mfma_f32_16x16x32_bf16 v[108:111], v[156:159], v[188:191], 0
	v_mfma_f32_16x16x32_bf16 v[96:99], v[142:145], v[196:199], 0
	v_mfma_f32_16x16x32_bf16 v[92:95], v[156:159], v[196:199], 0
	v_mfma_f32_16x16x32_bf16 v[80:83], v[142:145], v[204:207], 0
	v_mfma_f32_16x16x32_bf16 v[76:79], v[156:159], v[204:207], 0
	v_mfma_f32_16x16x32_bf16 v[128:131], v[152:155], v[184:187], v[128:131]
	v_mfma_f32_16x16x32_bf16 v[124:127], v[160:163], v[184:187], v[124:127]
	v_mfma_f32_16x16x32_bf16 v[112:115], v[152:155], v[192:195], v[112:115]
	v_mfma_f32_16x16x32_bf16 v[108:111], v[160:163], v[192:195], v[108:111]
	v_mfma_f32_16x16x32_bf16 v[96:99], v[152:155], v[200:203], v[96:99]
	v_mfma_f32_16x16x32_bf16 v[92:95], v[160:163], v[200:203], v[92:95]
	v_mfma_f32_16x16x32_bf16 v[80:83], v[152:155], v[208:211], v[80:83]
	v_mfma_f32_16x16x32_bf16 v[76:79], v[160:163], v[208:211], v[76:79]
	s_setprio 0
	s_setprio 1
	v_mfma_f32_16x16x32_bf16 v[120:123], v[164:167], v[180:183], 0
	v_mfma_f32_16x16x32_bf16 v[116:119], v[172:175], v[180:183], 0
	v_mfma_f32_16x16x32_bf16 v[104:107], v[164:167], v[188:191], 0
	v_mfma_f32_16x16x32_bf16 v[100:103], v[172:175], v[188:191], 0
	v_mfma_f32_16x16x32_bf16 v[88:91], v[164:167], v[196:199], 0
	v_mfma_f32_16x16x32_bf16 v[84:87], v[172:175], v[196:199], 0
	v_mfma_f32_16x16x32_bf16 v[72:75], v[164:167], v[204:207], 0
	v_mfma_f32_16x16x32_bf16 v[68:71], v[172:175], v[204:207], 0
	v_mfma_f32_16x16x32_bf16 v[120:123], v[168:171], v[184:187], v[120:123]
	v_mfma_f32_16x16x32_bf16 v[116:119], v[176:179], v[184:187], v[116:119]
	v_mfma_f32_16x16x32_bf16 v[104:107], v[168:171], v[192:195], v[104:107]
	v_mfma_f32_16x16x32_bf16 v[100:103], v[176:179], v[192:195], v[100:103]
	v_mfma_f32_16x16x32_bf16 v[88:91], v[168:171], v[200:203], v[88:91]
	v_mfma_f32_16x16x32_bf16 v[84:87], v[176:179], v[200:203], v[84:87]
	v_mfma_f32_16x16x32_bf16 v[72:75], v[168:171], v[208:211], v[72:75]
	v_mfma_f32_16x16x32_bf16 v[68:71], v[176:179], v[208:211], v[68:71]
	s_setprio 0
	s_barrier
	s_add_i32 s67, s67, s25
	v_lshl_add_u64 v[212:213], s[0:1], 0, v[2:3]
	s_mov_b32 m0, s67
	ds_read_b128 v[180:183], v150 offset:16384
	ds_read_b128 v[184:187], v150 offset:17408
	ds_read_b128 v[188:191], v150 offset:18432
	ds_read_b128 v[192:195], v150 offset:19456
	ds_read_b128 v[196:199], v150 offset:20480
	ds_read_b128 v[200:203], v150 offset:21504
	ds_read_b128 v[204:207], v150 offset:22528
	ds_read_b128 v[208:211], v150 offset:23552
	global_load_lds_dwordx4 v[212:213], off
	s_add_i32 m0, s67, 0x2000
	s_add_u32 s68, s0, 0x40000
	v_lshl_add_u64 v[214:215], s[0:1], 0, v[136:137]
	s_addc_u32 s69, s1, 0
	s_add_i32 s67, s70, s25
	global_load_lds_dwordx4 v[214:215], off
	v_lshl_add_u64 v[216:217], s[68:69], 0, v[2:3]
	s_mov_b32 m0, s67
	v_lshl_add_u64 v[218:219], s[28:29], 0, v[134:135]
	global_load_lds_dwordx4 v[216:217], off
	v_lshl_add_u64 v[216:217], s[68:69], 0, v[136:137]
	s_add_i32 m0, s67, 0x2000
	s_nop 0
	global_load_lds_dwordx4 v[216:217], off
	v_lshl_add_u64 v[216:217], s[28:29], 0, v[132:133]
	s_mov_b32 m0, s15
	s_nop 0
	global_load_lds_dwordx4 v[216:217], off
	s_mov_b32 m0, s21
	s_nop 0
	global_load_lds_dwordx4 v[218:219], off
	s_cmp_eq_u32 s32, 0
	s_cbranch_scc1 .Lpw_gu_2
	s_waitcnt vmcnt(16)
	s_branch .Lpj_gu_2
	.p2align 6
	s_nop 0
	s_nop 0
	s_nop 0
	s_nop 0
	s_nop 0
	s_nop 0
	s_nop 0
	s_nop 0
	s_nop 0
	s_nop 0
	s_nop 0
	s_nop 0
	s_nop 0

; __device__ __forceinline__ unsigned xb_ld(unsigned* p)              { return __hip_atomic_load(p, __ATOMIC_RELAXED, __HIP_MEMORY_SCOPE_AGENT); }
; __device__ __forceinline__ unsigned xb_add(unsigned* p, unsigned v) { return __hip_atomic_fetch_add(p, v, __ATOMIC_RELAXED, __HIP_MEMORY_SCOPE_AGENT); }
; #define XB_SPIN(cond, bar) do { unsigned _sp = 0; while (cond) { __builtin_amdgcn_s_sleep(1); \
;     if ((++_sp & 255u) == 0u) { if (xb_ld(&(bar)[XB_TMO])) break; if (_sp > XB_SPIN_CAP) { atomicAdd(&(bar)[XB_TMO], 1u); break; } } } } while (0)
; __device__ __forceinline__ void xcd_barrier(const XcdBarrier& b, const bool group_local = false, const bool xcc_only = false) {
;     ...
;         if (xcc_only && b.st[2] == 2u) {
;             if (old + 1u == (gen + 1u) * nloc) xb_add(&bar[XB_XGEN(b.x)], 1u);
;             else
;             XB_SPIN(xb_ld(&bar[XB_XSUB(b.x)]) < (gen + 1u) * nloc, bar);
;     ...
;             asm volatile("s_waitcnt vmcnt(0)" ::: "memory");
;     ...
;             __builtin_amdgcn_fence(__ATOMIC_ACQUIRE, "agent");
;             asm volatile("s_waitcnt vmcnt(0)" ::: "memory");
.LBB0_1729:
	s_add_u32 s4, s6, 0x2400
	s_addc_u32 s5, s7, 0
	v_mov_b64_e32 v[4:5], s[4:5]
	s_or_b64 s[12:13], s[12:13], exec
	s_or_b64 exec, exec, s[0:1]
	s_and_saveexec_b64 s[0:1], s[12:13]
	s_cbranch_execnz .LBB0_1427
	s_branch .LBB0_1428
	.p2align 6
	s_nop 0
	s_nop 0
	s_nop 0
	s_nop 0
	s_nop 0
	s_nop 0
	s_nop 0
	s_nop 0
	s_nop 0
